# baseline (speedup 1.0000x reference)
.LBB1_235:
	v_add_u32_e32 v0, s66, v0
	v_subrev_u32_e32 v0, 0x100, v0
	s_movk_i32 s0, 0xf0
	v_cmp_gt_u32_e32 vcc, s0, v0
	s_and_saveexec_b64 s[0:1], vcc
	s_cbranch_execz .Lepi_idle
	s_load_dwordx4 s[68:71], s[14:15], 0x0
	s_load_dwordx2 s[72:73], s[14:15], 0x10
	s_movk_i32 s0, 0x77
	v_mov_b32_e32 v1, 0xffffff88
	v_cmp_lt_u32_e32 vcc, s0, v0
	v_mov_b32_e32 v2, 0x44704000
	s_mov_b32 s0, 0xf800000
	v_cndmask_b32_e32 v1, 0, v1, vcc
	v_add_u32_e32 v0, v1, v0
	v_cvt_f32_u32_e32 v1, v0
	s_mov_b32 s5, 0x17800
	s_mov_b32 s4, 0x3eb17218
	v_fmac_f32_e32 v2, 0xc1000000, v1
	v_sqrt_f32_e32 v1, v2
	s_nop 0
	v_sub_f32_e32 v1, 0x41f80000, v1
	v_mul_f32_e32 v1, 0.5, v1
	v_cvt_i32_f32_e32 v1, v1
	s_and_b64 s[0:1], exec, s[16:17]
	s_cselect_b32 s2, s40, s38
	s_cselect_b32 s3, s39, s33
	v_sub_u32_e32 v2, 31, v1
	v_mul_u32_u24_e32 v2, v2, v1
	v_lshrrev_b32_e32 v3, 31, v2
	v_add_u32_e32 v2, v2, v3
	v_ashrrev_i32_e32 v2, 1, v2
	v_cmp_gt_i32_e64 s[0:1], v2, v0
	s_nop 1
	v_subbrev_co_u32_e64 v1, s[0:1], 0, v1, s[0:1]
	v_add_u32_e32 v2, 1, v1
	v_sub_u32_e32 v3, 30, v1
	v_mul_u32_u24_e32 v3, v2, v3
	v_lshrrev_b32_e32 v4, 31, v3
	v_add_u32_e32 v3, v3, v4
	v_ashrrev_i32_e32 v3, 1, v3
	v_cmp_gt_i32_e64 s[0:1], v3, v0
	s_nop 1
	v_cndmask_b32_e64 v12, v2, v1, s[0:1]
	v_sub_u32_e32 v1, 31, v12
	v_mul_u32_u24_e32 v1, v1, v12
	v_lshrrev_b32_e32 v2, 31, v1
	v_add_u32_e32 v1, v1, v2
	v_ashrrev_i32_e32 v1, 1, v1
	v_sub_u32_e32 v0, v0, v1
	v_cndmask_b32_e64 v1, 0, 16, vcc
	v_lshl_or_b32 v1, s2, 5, v1
	v_add_u32_e32 v1, v1, v12
	v_sub_u32_e32 v2, 0xff, v1
	v_mul_u32_u24_e32 v1, v2, v1
	v_lshrrev_b32_e32 v2, 31, v1
	v_add_u32_e32 v1, v1, v2
	v_ashrrev_i32_e32 v1, 1, v1
	v_add3_u32 v13, v12, v0, 1
	v_add_u32_e32 v0, v1, v0
	v_ashrrev_i32_e32 v1, 31, v0
	v_mov_b32_e32 v2, 0x1fc0
	v_mad_u64_u32 v[0:1], s[0:1], s3, v2, v[0:1]
	v_mad_u64_u32 v[4:5], s[0:1], v0, 24, s[10:11]
	v_mov_b32_e32 v0, 0x17800
	v_lshl_add_u32 v14, v12, 2, v0
	v_mov_b32_e32 v0, 0x60
	v_cndmask_b32_e32 v15, 0, v0, vcc
	v_or_b32_e32 v2, 16, v15
	v_add_lshl_u32 v3, v2, v12, 6
	v_add_u32_e32 v2, v2, v13
	v_lshl_add_u32 v6, v2, 6, v14
	v_add_u32_e32 v2, 32, v15
	v_add_lshl_u32 v7, v2, v12, 6
	v_add_u32_e32 v2, v2, v13
	v_lshl_add_u32 v8, v2, 6, v14
	v_add_u32_e32 v2, 48, v15
	v_mad_i32_i24 v5, v1, 24, v5
	v_add_lshl_u32 v0, v15, v12, 6
	v_lshlrev_b32_e32 v16, 2, v13
	v_add_u32_e32 v1, v15, v13
	v_add_lshl_u32 v9, v2, v12, 6
	v_add_u32_e32 v17, 64, v15
	v_add_u32_e32 v15, 0x50, v15
	v_add3_u32 v0, v0, v16, s5
	v_lshl_add_u32 v1, v1, 6, v14
	v_add3_u32 v3, v3, v16, s5
	v_add3_u32 v7, v7, v16, s5
	v_add3_u32 v9, v9, v16, s5
	v_add_u32_e32 v2, v2, v13
	v_add_lshl_u32 v18, v17, v12, 6
	v_add_lshl_u32 v12, v15, v12, 6
	v_lshl_add_u32 v10, v2, 6, v14
	ds_read_b32 v0, v0
	ds_read_b32 v2, v1
	ds_read_b32 v1, v3
	ds_read_b32 v3, v6
	ds_read_b32 v6, v7
	ds_read_b32 v8, v8
	ds_read_b32 v7, v9
	ds_read_b32 v9, v10
	v_add3_u32 v18, v18, v16, s5
	v_add3_u32 v16, v12, v16, s5
	v_add_u32_e32 v12, v15, v13
	v_add_u32_e32 v17, v17, v13
	v_lshl_add_u32 v15, v12, 6, v14
	v_lshl_add_u32 v17, v17, 6, v14
	ds_read_b32 v12, v18
	ds_read_b32 v14, v17
	ds_read_b32 v13, v16
	ds_read_b32 v15, v15
	s_waitcnt lgkmcnt(0)
	v_pk_add_f32 v[0:1], v[0:1], v[2:3]
	v_mov_b32_e32 v2, s70
	v_mov_b32_e32 v3, s71
	v_mov_b64_e32 v[10:11], s[68:69]
	v_pk_add_f32 v[6:7], v[6:7], v[8:9]
	v_pk_fma_f32 v[0:1], v[0:1], s[4:5], v[10:11] op_sel_hi:[1,0,1]
	v_pk_fma_f32 v[2:3], v[6:7], s[4:5], v[2:3] op_sel_hi:[1,0,1]
	global_store_dwordx4 v[4:5], v[0:3], off
	s_nop 1
	v_pk_add_f32 v[0:1], v[12:13], v[14:15]
	v_mov_b64_e32 v[2:3], s[72:73]
	v_pk_fma_f32 v[0:1], v[0:1], s[4:5], v[2:3] op_sel_hi:[1,0,1]
	global_store_dwordx2 v[4:5], v[0:1], off offset:16
	s_endpgm
